# queue-index prefetch: next item's claiming atomic issued one item early for gdn_prep, ret_kv, prep_tok and cvt_early queues
# baseline (speedup 1.0000x reference)
_Z10fwd_kernel6Params:
	s_mov_b32 s100, 1
	v_writelane_b32 v255, s100, 13
	s_mov_b32 s100, 0
	v_writelane_b32 v255, s100, 7
	s_mov_b32 s100, 0
	v_writelane_b32 v255, s100, 9
	s_mov_b32 s88, s2
	s_load_dword s2, s[0:1], 0xc0
	v_cmp_gt_u32_e32 vcc, 16, v0
	s_waitcnt lgkmcnt(0)
	v_writelane_b32 v252, s2, 0
	s_add_u32 s2, s0, 0xc0
	s_addc_u32 s3, s1, 0
	v_writelane_b32 v252, s2, 1
	s_nop 1
	v_writelane_b32 v252, s3, 2
	s_and_saveexec_b64 s[2:3], vcc
	v_lshl_add_u32 v1, v0, 2, 0
	v_add_u32_e32 v1, 0x21000, v1
	v_mov_b32_e32 v2, 0
	ds_write_b32 v1, v2
	s_or_b64 exec, exec, s[2:3]
	s_load_dwordx4 s[84:87], s[0:1], 0xa8
	v_cmp_gt_u32_e32 vcc, 21, v0
	s_and_saveexec_b64 s[2:3], vcc
	s_cbranch_execz .LBB0_4
	v_lshlrev_b32_e32 v1, 3, v0
	global_load_dwordx2 v[2:3], v1, s[0:1]
	v_add_u32_e32 v1, 0, v1
	v_add_u32_e32 v1, 0x21040, v1
	s_waitcnt vmcnt(0)
	ds_write_b64 v1, v[2:3]

.LBB0_257:
	s_waitcnt lgkmcnt(0)
	s_barrier
	s_and_saveexec_b64 s[0:1], s[36:37]
	s_cbranch_execz .LBB0_259
	v_mov_b64_e32 v[4:5], s[8:9]
	v_mov_b32_e32 v2, s23
	v_readlane_b32 s100, v255, 13
	s_cmp_eq_u32 s100, s8
	s_cbranch_scc1 .Lqp_have_gdn_prep
	s_waitcnt vmcnt(0)
	global_atomic_add v255, v[4:5], v228, off sc0
	v_writelane_b32 v255, s8, 13
.Lqp_have_gdn_prep:
	s_waitcnt vmcnt(0) lgkmcnt(0)
	ds_write_b32 v2, v255
	global_atomic_add v255, v[4:5], v228, off sc0

.LBB0_379:
	s_waitcnt lgkmcnt(0)
	s_barrier
	s_and_saveexec_b64 s[8:9], s[0:1]
	s_cbranch_execz .LBB0_381
	v_mov_b64_e32 v[4:5], s[4:5]
	v_mov_b32_e32 v2, s2
	v_readlane_b32 s100, v255, 13
	s_cmp_eq_u32 s100, s4
	s_cbranch_scc1 .Lqp_have_ret_kv
	s_waitcnt vmcnt(0)
	global_atomic_add v255, v[4:5], v228, off sc0
	v_writelane_b32 v255, s4, 13

.LBB0_386:
	s_waitcnt lgkmcnt(0)
	s_barrier
	s_and_saveexec_b64 s[4:5], s[36:37]
	s_cbranch_execz .LBB0_388
	v_mov_b64_e32 v[4:5], s[0:1]
	v_mov_b32_e32 v2, s2
	v_readlane_b32 s100, v255, 13
	s_cmp_eq_u32 s100, s0
	s_cbranch_scc1 .Lqp_have_prep_tok
	s_waitcnt vmcnt(0)
	global_atomic_add v255, v[4:5], v228, off sc0
	v_writelane_b32 v255, s0, 13

.LBB0_1328:
	s_waitcnt lgkmcnt(0)
	s_barrier
	s_and_saveexec_b64 s[0:1], s[36:37]
	s_cbranch_execz .LBB0_1330
	v_mov_b64_e32 v[4:5], s[4:5]
	v_mov_b32_e32 v2, s33
	v_readlane_b32 s100, v255, 13
	s_cmp_eq_u32 s100, s4
	s_cbranch_scc1 .Lqp_have_cvt_early
	s_waitcnt vmcnt(0)
	global_atomic_add v255, v[4:5], v228, off sc0
	v_writelane_b32 v255, s4, 13
